# speedup vs baseline: 1.0151x; 1.0021x over previous
.LBB0_45:
	global_load_dword v5, v[2:3], off
	v_add_u32_e32 v4, 0x200, v4
	v_cmp_lt_u32_e32 vcc, s4, v4
	v_lshl_add_u64 v[2:3], v[2:3], 0, 32
	s_or_b64 s[0:1], vcc, s[0:1]
	s_waitcnt vmcnt(0)
	v_cvt_f16_f32_e32 v5, v5
	global_store_short v[0:1], v5, off sc1
	v_lshl_add_u64 v[0:1], v[0:1], 0, s[2:3]
	s_andn2_b64 exec, exec, s[0:1]
	s_cbranch_execnz .LBB0_45

.LBB0_47:
	s_load_dwordx2 s[4:5], s[0:1], 0x18
	ds_read_b32 v1, v1 offset:1564
	s_mul_i32 s11, s2, 0x188
	v_add_u32_e32 v26, s11, v0
	v_mov_b32_e32 v27, 0
	s_waitcnt lgkmcnt(0)
	v_lshl_add_u64 v[26:27], v[26:27], 2, s[4:5]
	global_store_dword v[26:27], v1, off sc1
	s_or_b64 exec, exec, s[8:9]
	s_load_dwordx2 s[4:5], s[0:1], 0x20
	s_and_saveexec_b64 s[8:9], s[6:7]
	s_cbranch_execz .LBB0_33

.LBB1_13:
	v_add_u32_e32 v6, v5, v4
	v_ashrrev_i32_e32 v6, 1, v6
	v_lshlrev_b32_e32 v7, 2, v6
	ds_read_b32 v7, v7
	s_add_i32 s12, s12, -1
	s_cmp_lg_u32 s12, 0
	s_waitcnt lgkmcnt(0)
	v_cmp_gt_i32_e32 vcc, v7, v3
	s_nop 1
	v_cndmask_b32_e32 v5, v5, v6, vcc
	v_cndmask_b32_e32 v4, v6, v4, vcc
	s_cbranch_scc1 .LBB1_13
	v_lshlrev_b32_e32 v4, 2, v4
	ds_read_b32 v5, v4 offset:1568
	ds_read_b32 v4, v4
	s_waitcnt lgkmcnt(1)
	v_add_u32_e32 v5, v5, v3
	s_waitcnt lgkmcnt(0)
	v_sub_u32_e32 v4, v5, v4
	v_ashrrev_i32_e32 v5, 31, v4
	v_lshl_add_u64 v[4:5], v[4:5], 3, s[8:9]
	global_load_dwordx2 v[4:5], v[4:5], off
	v_add_u32_e32 v3, 0x200, v3
	v_cmp_le_i32_e32 vcc, s33, v3
	s_or_b64 s[10:11], vcc, s[10:11]
	s_waitcnt vmcnt(0)
	v_lshrrev_b32_e32 v4, 15, v4
	v_and_b32_e32 v4, 0x1fffc, v4
	ds_add_u32 v4, v2 offset:3132
	ds_add_f32 v4, v5 offset:8192
	s_andn2_b64 exec, exec, s[10:11]
	s_cbranch_execnz .LBB1_12
	s_or_b64 exec, exec, s[10:11]
	v_mov_b32_e32 v4, 0
	s_waitcnt lgkmcnt(0)
	s_barrier
	s_and_saveexec_b64 s[10:11], s[4:5]
	ds_read_b32 v4, v1 offset:3132
	s_or_b64 exec, exec, s[10:11]
	s_waitcnt lgkmcnt(0)
	v_add_u32_dpp v2, v4, v4 row_shr:1 row_mask:0xf bank_mask:0xf bound_ctrl:1
	s_nop 1
	v_add_u32_dpp v2, v2, v2 row_shr:2 row_mask:0xf bank_mask:0xf bound_ctrl:1
	s_nop 1
	v_add_u32_dpp v2, v2, v2 row_shr:4 row_mask:0xf bank_mask:0xf bound_ctrl:1
	s_nop 1
	v_add_u32_dpp v5, v2, v2 row_shr:8 row_mask:0xf bank_mask:0xf bound_ctrl:1
	s_nop 1
	v_add_u32_dpp v5, v5, v5 row_bcast:15 row_mask:0xa bank_mask:0xf
	s_nop 1
	v_add_u32_dpp v5, v5, v5 row_bcast:31 row_mask:0xc bank_mask:0xf
	s_and_saveexec_b64 s[10:11], s[6:7]
	v_lshlrev_b32_e32 v2, 2, v20
	ds_write_b32 v2, v5 offset:4156
	s_or_b64 exec, exec, s[10:11]
	v_mov_b32_e32 v2, 0x103c
	v_mov_b32_e32 v6, 0
	s_waitcnt lgkmcnt(0)
	s_barrier
	ds_read2_b32 v[2:3], v2 offset1:1
	ds_read_b32 v6, v6 offset:4164
	s_waitcnt lgkmcnt(0)
	s_barrier
	s_and_saveexec_b64 s[10:11], s[4:5]
	s_cbranch_execz .LBB1_23
	v_cmp_lt_u32_e32 vcc, 63, v0
	s_movk_i32 s12, 0x7f
	v_sub_u32_e32 v4, s34, v4
	v_cndmask_b32_e32 v7, 0, v2, vcc
	v_cmp_lt_u32_e32 vcc, s12, v0
	s_movk_i32 s12, 0xbf
	v_lshl_or_b32 v2, s35, 8, v0
	v_cndmask_b32_e32 v3, 0, v3, vcc
	v_cmp_lt_u32_e32 vcc, s12, v0
	s_mov_b32 s12, 0x186a0
	v_add3_u32 v4, v4, v5, v7
	v_cndmask_b32_e32 v6, 0, v6, vcc
	v_cmp_gt_u32_e32 vcc, s12, v2
	v_add3_u32 v4, v4, v3, v6
	s_and_saveexec_b64 s[12:13], vcc
	s_cbranch_execz .LBB1_22
	ds_read_b32 v5, v1 offset:8192
	s_mov_b32 s14, 0x800000
	v_mov_b32_e32 v3, 0
	v_lshlrev_b64 v[2:3], 2, v[2:3]
	s_waitcnt lgkmcnt(0)
	v_add_f32_e32 v5, 1.0, v5
	v_mul_f32_e32 v6, 0x4b800000, v5
	v_cmp_gt_f32_e32 vcc, s14, v5
	s_nop 1
	v_cndmask_b32_e32 v6, v5, v6, vcc
	v_rsq_f32_e32 v8, v6
	v_lshl_add_u64 v[6:7], s[26:27], 0, v[2:3]
	global_store_dword v[6:7], v4, off sc1
	v_lshl_add_u64 v[2:3], s[28:29], 0, v[2:3]
	v_mul_f32_e32 v6, 0x45800000, v8
	v_cndmask_b32_e32 v6, v8, v6, vcc
	v_cmp_lt_f32_e32 vcc, 0, v5
	s_nop 1
	v_cndmask_b32_e32 v5, 0, v6, vcc
	global_store_dword v[2:3], v5, off sc1
	ds_write_b32 v1, v5 offset:4220

.LBB1_23:
	s_or_b64 exec, exec, s[10:11]
	s_cmpk_eq_i32 s35, 0x186
	s_cselect_b64 s[10:11], -1, 0
	s_and_b64 s[12:13], s[2:3], s[10:11]
	s_and_saveexec_b64 s[10:11], s[12:13]
	s_cbranch_execz .LBB1_25
	v_mov_b32_e32 v2, 0x61000
	v_mov_b32_e32 v3, 0x186a00
	global_store_dword v2, v3, s[26:27] offset:2688 sc1

.LBB1_27:
	v_add_u32_e32 v6, v5, v4
	v_ashrrev_i32_e32 v6, 1, v6
	v_lshlrev_b32_e32 v7, 2, v6
	ds_read_b32 v7, v7
	s_add_i32 s13, s13, -1
	s_cmp_lg_u32 s13, 0
	s_waitcnt lgkmcnt(0)
	v_cmp_gt_i32_e32 vcc, v7, v3
	s_nop 1
	v_cndmask_b32_e32 v5, v5, v6, vcc
	v_cndmask_b32_e32 v4, v6, v4, vcc
	s_cbranch_scc1 .LBB1_27
	v_lshlrev_b32_e32 v4, 2, v4
	ds_read_b32 v5, v4 offset:1568
	ds_read_b32 v4, v4
	s_waitcnt lgkmcnt(1)
	v_add_u32_e32 v5, v5, v3
	s_waitcnt lgkmcnt(0)
	v_sub_u32_e32 v4, v5, v4
	v_ashrrev_i32_e32 v5, 31, v4
	v_lshl_add_u64 v[4:5], v[4:5], 3, s[8:9]
	global_load_dwordx2 v[4:5], v[4:5], off
	v_add_u32_e32 v3, 0x200, v3
	v_cmp_le_i32_e32 vcc, s33, v3
	s_or_b64 s[10:11], vcc, s[10:11]
	s_waitcnt vmcnt(0)
	v_lshrrev_b32_e32 v6, 15, v4
	v_and_b32_e32 v6, 0x1fffc, v6
	ds_add_rtn_u32 v6, v6, v2 offset:3132
	v_cvt_f16_f32_sdwa v5, v5 dst_sel:WORD_1 dst_unused:UNUSED_PAD src0_sel:DWORD
	s_waitcnt lgkmcnt(0)
	v_ashrrev_i32_e32 v7, 31, v6
	v_add_u32_e32 v5, 0x10000, v5
	v_bfi_b32 v8, s12, v5, v4
	v_lshl_add_u64 v[4:5], v[6:7], 2, s[24:25]
	global_store_dword v[4:5], v8, off sc1
	s_andn2_b64 exec, exec, s[10:11]
	s_cbranch_execnz .LBB1_26
	s_or_b64 exec, exec, s[10:11]
	s_lshl_b32 s14, s35, 8
	v_or_b32_e32 v23, 0x200, v0
	v_or_b32_e32 v22, 0x600, v0
	s_branch .LBB1_100

.LBB1_80:
	s_or_b64 exec, exec, s[6:7]
	v_add_f32_e32 v4, v4, v5
	v_add_f32_e32 v2, v2, v3
	s_lshl_b32 s14, s35, 8
	v_add_f32_e32 v3, v2, v4
	v_or_b32_e32 v2, s14, v7
	s_mov_b32 s6, 0x186a0
	v_cmp_eq_u32_e64 s[4:5], 0, v8
	v_cmp_gt_u32_e64 s[6:7], s6, v2
	v_mov_b32_dpp v4, v3 quad_perm:[1,0,3,2] row_mask:0xf bank_mask:0xf bound_ctrl:1
	s_and_b64 s[4:5], s[4:5], s[6:7]
	s_and_saveexec_b64 s[6:7], s[4:5]
	s_cbranch_execz .LBB1_82
	v_add_f32_e32 v3, v3, v4
	v_add_f32_e32 v7, 1.0, v3
	s_mov_b32 s4, 0x800000
	v_mul_f32_e32 v4, 0x4b800000, v7
	v_cmp_gt_f32_e64 s[4:5], s4, v7
	v_mov_b32_e32 v3, 0
	v_lshlrev_b64 v[2:3], 2, v[2:3]
	v_cndmask_b32_e64 v4, v7, v4, s[4:5]
	v_rsq_f32_e32 v8, v4
	v_add_u32_e32 v6, s34, v6
	v_lshl_add_u64 v[4:5], s[26:27], 0, v[2:3]
	global_store_dword v[4:5], v6, off sc1
	v_mul_f32_e32 v4, 0x45800000, v8
	v_cndmask_b32_e64 v4, v8, v4, s[4:5]
	v_cmp_lt_f32_e64 s[4:5], 0, v7
	v_lshl_add_u64 v[2:3], s[28:29], 0, v[2:3]
	s_nop 0
	v_cndmask_b32_e64 v4, 0, v4, s[4:5]
	global_store_dword v[2:3], v4, off sc1
	ds_write_b32 v1, v4 offset:4220
.LBB1_82:
	s_or_b64 exec, exec, s[6:7]
	s_cmpk_eq_i32 s35, 0x186
	s_cselect_b64 s[4:5], -1, 0
	s_and_b64 s[4:5], s[2:3], s[4:5]
	s_and_saveexec_b64 s[2:3], s[4:5]
	s_cbranch_execz .LBB1_84
	v_mov_b32_e32 v1, 0x61000
	v_mov_b32_e32 v2, 0x186a00
	global_store_dword v1, v2, s[26:27] offset:2688 sc1
